# P11: 2^-5 output scale folded into the MFMA block scale (epilogue multiplies and zero-movs removed), on top of the ring attention loop
# baseline (speedup 1.0000x reference)
.LBB0_1138:
	s_add_u32 s6, s6, 0x1ce00000
	s_addc_u32 s7, s7, 0
	s_lshl_b32 s8, s8, 5
	s_lshl_b32 s57, s9, 6
	s_lshl_b32 s13, s9, 13
	s_and_b32 s58, s8, 0x60
	s_mov_b64 s[8:9], 0x80
	s_add_i32 m0, s29, 0x18000
	v_lshl_add_u64 v[8:9], v[8:9], 0, s[8:9]
	s_lshl_b32 s16, s58, 7
	s_waitcnt vmcnt(2)
	s_barrier
	global_load_lds_dwordx4 v[8:9], off
	v_lshl_add_u64 v[6:7], v[6:7], 0, s[8:9]
	s_add_i32 m0, s29, 0x1a000
	s_add_i32 s59, s29, 0x8000
	s_add_i32 s60, s29, 0xa000
	global_load_lds_dwordx4 v[6:7], off
	v_lshl_add_u64 v[4:5], v[4:5], 0, s[8:9]
	s_mov_b32 m0, s59
	s_add_u32 s14, s30, 0x10080
	global_load_lds_dwordx4 v[4:5], off
	v_lshl_add_u64 v[2:3], v[2:3], 0, s[8:9]
	s_mov_b32 m0, s60
	s_addc_u32 s15, s31, 0
	global_load_lds_dwordx4 v[2:3], off
	s_add_i32 m0, s29, 0x1c000
	v_lshl_add_u64 v[2:3], s[14:15], 0, v[164:165]
	global_load_lds_dwordx4 v[2:3], off
	v_lshl_add_u64 v[2:3], s[14:15], 0, v[162:163]
	s_add_i32 m0, s29, 0x1e000
	v_bfe_u32 v183, v10, 4, 2
	global_load_lds_dwordx4 v[2:3], off
	v_and_b32_e32 v182, 15, v10
	v_lshlrev_b32_e32 v2, 4, v183
	v_lshlrev_b32_e32 v4, 2, v10
	v_lshl_or_b32 v3, v182, 6, v2
	v_and_b32_e32 v4, 32, v4
	v_bitop3_b32 v3, v3, s13, v4 bitop3:0xde
	v_lshlrev_b32_e32 v5, 6, v10
	s_movk_i32 s13, 0x3c0
	v_and_or_b32 v2, v5, s13, v2
	s_waitcnt vmcnt(6)
	v_bitop3_b32 v184, s16, v2, v4 bitop3:0xf6
	s_or_b32 s62, s10, s12
	s_add_i32 s10, 0, 0x20144
	s_add_i32 s63, 0, 0x10000
	s_add_i32 s64, 0, 0x14000
	v_mov_b32_e32 v171, v165
	v_mov_b32_e32 v173, v165
	s_mov_b32 s61, 0
	v_mov_b32_e32 v185, s10
	v_add_u32_e32 v186, s63, v184
	v_add_u32_e32 v187, s64, v184
	v_add_u32_e32 v188, 0, v3
	v_mov_b32_e32 v189, 0x7f7f7f7f
	v_mov_b32_e32 v244, 0x7a7a7a7a
	s_mov_b32 s10, 0x3d000000
	s_mov_b64 s[12:13], 0x40000
	s_mov_b32 s65, 0x40000
	s_mov_b64 s[14:15], 0x50000
	s_mov_b32 s66, 0x50000
	s_barrier

.LBB0_1144:
	s_add_u32 s17, s34, s42
	s_addc_u32 s19, s35, s43
	s_add_u32 s21, s17, 0x100
	s_addc_u32 s44, s19, 0
	s_and_b64 s[40:41], s[38:39], exec
	s_cselect_b32 s40, s24, s21
	s_cselect_b32 s41, s25, s44
	s_add_u32 s21, s30, s42
	s_addc_u32 s42, s31, s43
	s_add_u32 s21, s21, 0x100
	s_addc_u32 s42, s42, 0
	ds_read_b128 v[18:21], v186
	ds_read_b128 v[22:25], v186 offset:1024
	ds_read_b128 v[26:29], v186 offset:2048
	ds_read_b128 v[30:33], v186 offset:3072
	ds_read_b128 v[2:5], v187
	ds_read_b128 v[6:9], v187 offset:1024
	ds_read_b128 v[10:13], v187 offset:2048
	ds_read_b128 v[14:17], v187 offset:3072
	s_and_b64 s[38:39], s[38:39], exec
	s_cselect_b32 s43, s27, s42
	s_cselect_b32 s42, s26, s21
	s_add_u32 s46, s17, 0x80
	s_addc_u32 s47, s19, 0
	s_add_i32 s74, s63, s52
	s_add_i32 m0, s29, 0xc000
	s_add_i32 s75, s29, 0xe000
	s_add_i32 s71, s74, 0x2000
	s_add_u32 s44, s42, 0x10000
	s_addc_u32 s45, s43, 0
	s_add_i32 s70, 0, 0x18000
	s_add_i32 s73, s64, s52
	s_add_i32 s68, s70, s52
	s_add_i32 s72, s73, 0x2000
	s_add_i32 s69, 0, 0x1c000
	s_add_i32 s17, s68, 0x2000
	s_add_u32 s38, s42, 0x10080
	s_addc_u32 s39, s43, 0
	s_add_i32 s21, s69, s52
	s_add_i32 s19, s21, 0x2000
	v_lshl_add_u64 v[214:215], s[46:47], 0, v[170:171]
	ds_read_b128 v[174:177], v188
	ds_read_b128 v[178:181], v188 offset:1024
	ds_read_b128 v[190:193], v188 offset:2048
	ds_read_b128 v[194:197], v188 offset:3072
	ds_read_b128 v[198:201], v188 offset:4096
	ds_read_b128 v[202:205], v188 offset:5120
	ds_read_b128 v[206:209], v188 offset:6144
	ds_read_b128 v[210:213], v188 offset:7168
	global_load_lds_dwordx4 v[214:215], off
	v_lshl_add_u64 v[214:215], s[46:47], 0, v[172:173]
	s_mov_b32 m0, s75
	s_nop 0
	global_load_lds_dwordx4 v[214:215], off
	s_waitcnt vmcnt(8)
	s_waitcnt lgkmcnt(0)
	s_barrier
	s_setprio 1
	s_waitcnt lgkmcnt(0)
	v_mfma_scale_f32_16x16x128_f8f6f4 v[158:161], v[18:25], v[174:181], v[158:161], v244, v189 op_sel_hi:[0,0,0]
	v_mfma_scale_f32_16x16x128_f8f6f4 v[154:157], v[26:33], v[174:181], v[154:157], v244, v189 op_sel_hi:[0,0,0]
	v_mfma_scale_f32_16x16x128_f8f6f4 v[150:153], v[18:25], v[190:197], v[150:153], v244, v189 op_sel_hi:[0,0,0]
	v_mfma_scale_f32_16x16x128_f8f6f4 v[146:149], v[26:33], v[190:197], v[146:149], v244, v189 op_sel_hi:[0,0,0]
	v_mfma_scale_f32_16x16x128_f8f6f4 v[126:129], v[18:25], v[198:205], v[126:129], v244, v189 op_sel_hi:[0,0,0]
	v_mfma_scale_f32_16x16x128_f8f6f4 v[122:125], v[26:33], v[198:205], v[122:125], v244, v189 op_sel_hi:[0,0,0]
	v_mfma_scale_f32_16x16x128_f8f6f4 v[118:121], v[18:25], v[206:213], v[118:121], v244, v189 op_sel_hi:[0,0,0]
	v_mfma_scale_f32_16x16x128_f8f6f4 v[114:117], v[26:33], v[206:213], v[114:117], v244, v189 op_sel_hi:[0,0,0]
	s_setprio 0
	s_setprio 1
	v_mfma_scale_f32_16x16x128_f8f6f4 v[142:145], v[2:9], v[174:181], v[142:145], v244, v189 op_sel_hi:[0,0,0]
	v_mfma_scale_f32_16x16x128_f8f6f4 v[138:141], v[10:17], v[174:181], v[138:141], v244, v189 op_sel_hi:[0,0,0]
	v_mfma_scale_f32_16x16x128_f8f6f4 v[134:137], v[2:9], v[190:197], v[134:137], v244, v189 op_sel_hi:[0,0,0]
	v_mfma_scale_f32_16x16x128_f8f6f4 v[130:133], v[10:17], v[190:197], v[130:133], v244, v189 op_sel_hi:[0,0,0]
	v_mfma_scale_f32_16x16x128_f8f6f4 v[110:113], v[2:9], v[198:205], v[110:113], v244, v189 op_sel_hi:[0,0,0]
	v_mfma_scale_f32_16x16x128_f8f6f4 v[106:109], v[10:17], v[198:205], v[106:109], v244, v189 op_sel_hi:[0,0,0]
	v_mfma_scale_f32_16x16x128_f8f6f4 v[102:105], v[2:9], v[206:213], v[102:105], v244, v189 op_sel_hi:[0,0,0]
	v_mfma_scale_f32_16x16x128_f8f6f4 v[98:101], v[10:17], v[206:213], v[98:101], v244, v189 op_sel_hi:[0,0,0]
	s_setprio 0
	s_barrier
	s_mov_b32 m0, s74
	v_lshl_add_u64 v[174:175], s[42:43], 0, v[164:165]
	ds_read_b128 v[190:193], v188 offset:16384
	ds_read_b128 v[194:197], v188 offset:17408
	ds_read_b128 v[198:201], v188 offset:18432
	ds_read_b128 v[202:205], v188 offset:19456
	ds_read_b128 v[206:209], v188 offset:20480
	ds_read_b128 v[210:213], v188 offset:21504
	ds_read_b128 v[214:217], v188 offset:22528
	ds_read_b128 v[218:221], v188 offset:23552
	global_load_lds_dwordx4 v[174:175], off
	v_lshl_add_u64 v[176:177], s[42:43], 0, v[162:163]
	s_mov_b32 m0, s71
	v_lshl_add_u64 v[178:179], s[44:45], 0, v[164:165]
	global_load_lds_dwordx4 v[176:177], off
	s_mov_b32 m0, s73
	v_lshl_add_u64 v[180:181], s[40:41], 0, v[168:169]
	global_load_lds_dwordx4 v[178:179], off
	v_lshl_add_u64 v[178:179], s[44:45], 0, v[162:163]
	s_mov_b32 m0, s72
	s_nop 0
	global_load_lds_dwordx4 v[178:179], off
	v_lshl_add_u64 v[178:179], s[40:41], 0, v[166:167]
	s_mov_b32 m0, s29
	s_nop 0
	global_load_lds_dwordx4 v[178:179], off
	s_mov_b32 m0, s53
	s_nop 0
	global_load_lds_dwordx4 v[180:181], off
	s_waitcnt vmcnt(8)
	s_waitcnt lgkmcnt(0)
	s_barrier
	s_setprio 1
	s_waitcnt lgkmcnt(0)
	v_mfma_scale_f32_16x16x128_f8f6f4 v[78:81], v[18:25], v[190:197], v[78:81], v244, v189 op_sel_hi:[0,0,0]
	v_mfma_scale_f32_16x16x128_f8f6f4 v[74:77], v[26:33], v[190:197], v[74:77], v244, v189 op_sel_hi:[0,0,0]
	v_mfma_scale_f32_16x16x128_f8f6f4 v[70:73], v[18:25], v[198:205], v[70:73], v244, v189 op_sel_hi:[0,0,0]
	v_mfma_scale_f32_16x16x128_f8f6f4 v[66:69], v[26:33], v[198:205], v[66:69], v244, v189 op_sel_hi:[0,0,0]
	v_mfma_scale_f32_16x16x128_f8f6f4 v[46:49], v[18:25], v[206:213], v[46:49], v244, v189 op_sel_hi:[0,0,0]
	v_mfma_scale_f32_16x16x128_f8f6f4 v[42:45], v[26:33], v[206:213], v[42:45], v244, v189 op_sel_hi:[0,0,0]
	v_mfma_scale_f32_16x16x128_f8f6f4 v[38:41], v[18:25], v[214:221], v[38:41], v244, v189 op_sel_hi:[0,0,0]
	v_mfma_scale_f32_16x16x128_f8f6f4 v[34:37], v[26:33], v[214:221], v[34:37], v244, v189 op_sel_hi:[0,0,0]
	s_setprio 0
	s_setprio 1
	v_mfma_scale_f32_16x16x128_f8f6f4 v[90:93], v[2:9], v[190:197], v[90:93], v244, v189 op_sel_hi:[0,0,0]
	v_mfma_scale_f32_16x16x128_f8f6f4 v[94:97], v[10:17], v[190:197], v[94:97], v244, v189 op_sel_hi:[0,0,0]
	v_mfma_scale_f32_16x16x128_f8f6f4 v[82:85], v[2:9], v[198:205], v[82:85], v244, v189 op_sel_hi:[0,0,0]
	v_mfma_scale_f32_16x16x128_f8f6f4 v[86:89], v[10:17], v[198:205], v[86:89], v244, v189 op_sel_hi:[0,0,0]
	v_mfma_scale_f32_16x16x128_f8f6f4 v[58:61], v[2:9], v[206:213], v[58:61], v244, v189 op_sel_hi:[0,0,0]
	v_mfma_scale_f32_16x16x128_f8f6f4 v[62:65], v[10:17], v[206:213], v[62:65], v244, v189 op_sel_hi:[0,0,0]
	v_mfma_scale_f32_16x16x128_f8f6f4 v[50:53], v[2:9], v[214:221], v[50:53], v244, v189 op_sel_hi:[0,0,0]
	v_mfma_scale_f32_16x16x128_f8f6f4 v[54:57], v[10:17], v[214:221], v[54:57], v244, v189 op_sel_hi:[0,0,0]
	s_setprio 0
	s_barrier
	v_add_u32_e32 v14, s70, v184
	v_add_u32_e32 v30, s69, v184
	ds_read_b128 v[2:5], v14
	ds_read_b128 v[6:9], v14 offset:1024
	ds_read_b128 v[10:13], v14 offset:2048
	ds_read_b128 v[14:17], v14 offset:3072
	ds_read_b128 v[18:21], v30
	ds_read_b128 v[22:25], v30 offset:1024
	ds_read_b128 v[26:29], v30 offset:2048
	ds_read_b128 v[30:33], v30 offset:3072
	s_mov_b32 m0, s54
	v_lshl_add_u64 v[222:223], s[40:41], 0, v[170:171]
	ds_read_b128 v[190:193], v188 offset:32768
	ds_read_b128 v[194:197], v188 offset:33792
	ds_read_b128 v[198:201], v188 offset:34816
	ds_read_b128 v[202:205], v188 offset:35840
	ds_read_b128 v[206:209], v188 offset:36864
	ds_read_b128 v[210:213], v188 offset:37888
	ds_read_b128 v[214:217], v188 offset:38912
	ds_read_b128 v[218:221], v188 offset:39936
	global_load_lds_dwordx4 v[222:223], off
	v_lshl_add_u64 v[222:223], s[40:41], 0, v[172:173]
	s_mov_b32 m0, s55
	s_nop 0
	global_load_lds_dwordx4 v[222:223], off
	s_waitcnt vmcnt(8)
	s_waitcnt lgkmcnt(0)
	s_barrier
	s_setprio 1
	s_waitcnt lgkmcnt(0)
	v_mfma_scale_f32_16x16x128_f8f6f4 v[158:161], v[2:9], v[190:197], v[158:161], v244, v189 op_sel_hi:[0,0,0]
	v_mfma_scale_f32_16x16x128_f8f6f4 v[154:157], v[10:17], v[190:197], v[154:157], v244, v189 op_sel_hi:[0,0,0]
	v_mfma_scale_f32_16x16x128_f8f6f4 v[150:153], v[2:9], v[198:205], v[150:153], v244, v189 op_sel_hi:[0,0,0]
	v_mfma_scale_f32_16x16x128_f8f6f4 v[146:149], v[10:17], v[198:205], v[146:149], v244, v189 op_sel_hi:[0,0,0]
	v_mfma_scale_f32_16x16x128_f8f6f4 v[126:129], v[2:9], v[206:213], v[126:129], v244, v189 op_sel_hi:[0,0,0]
	v_mfma_scale_f32_16x16x128_f8f6f4 v[122:125], v[10:17], v[206:213], v[122:125], v244, v189 op_sel_hi:[0,0,0]
	v_mfma_scale_f32_16x16x128_f8f6f4 v[118:121], v[2:9], v[214:221], v[118:121], v244, v189 op_sel_hi:[0,0,0]
	v_mfma_scale_f32_16x16x128_f8f6f4 v[114:117], v[10:17], v[214:221], v[114:117], v244, v189 op_sel_hi:[0,0,0]
	s_setprio 0
	s_setprio 1
	v_mfma_scale_f32_16x16x128_f8f6f4 v[142:145], v[18:25], v[190:197], v[142:145], v244, v189 op_sel_hi:[0,0,0]
	v_mfma_scale_f32_16x16x128_f8f6f4 v[138:141], v[26:33], v[190:197], v[138:141], v244, v189 op_sel_hi:[0,0,0]
	v_mfma_scale_f32_16x16x128_f8f6f4 v[134:137], v[18:25], v[198:205], v[134:137], v244, v189 op_sel_hi:[0,0,0]
	v_mfma_scale_f32_16x16x128_f8f6f4 v[130:133], v[26:33], v[198:205], v[130:133], v244, v189 op_sel_hi:[0,0,0]
	v_mfma_scale_f32_16x16x128_f8f6f4 v[110:113], v[18:25], v[206:213], v[110:113], v244, v189 op_sel_hi:[0,0,0]
	v_mfma_scale_f32_16x16x128_f8f6f4 v[106:109], v[26:33], v[206:213], v[106:109], v244, v189 op_sel_hi:[0,0,0]
	v_mfma_scale_f32_16x16x128_f8f6f4 v[102:105], v[18:25], v[214:221], v[102:105], v244, v189 op_sel_hi:[0,0,0]
	v_mfma_scale_f32_16x16x128_f8f6f4 v[98:101], v[26:33], v[214:221], v[98:101], v244, v189 op_sel_hi:[0,0,0]
	s_setprio 0
	s_barrier
	s_mov_b32 m0, s68
	v_lshl_add_u64 v[174:175], v[174:175], 0, s[8:9]
	ds_read_b128 v[190:193], v188 offset:49152
	ds_read_b128 v[194:197], v188 offset:50176
	ds_read_b128 v[198:201], v188 offset:51200
	ds_read_b128 v[202:205], v188 offset:52224
	ds_read_b128 v[206:209], v188 offset:53248
	ds_read_b128 v[210:213], v188 offset:54272
	ds_read_b128 v[214:217], v188 offset:55296
	ds_read_b128 v[218:221], v188 offset:56320
	global_load_lds_dwordx4 v[174:175], off
	v_lshl_add_u64 v[174:175], v[176:177], 0, s[8:9]
	s_mov_b32 m0, s17
	s_nop 0
	global_load_lds_dwordx4 v[174:175], off
	v_lshl_add_u64 v[174:175], s[38:39], 0, v[164:165]
	s_mov_b32 m0, s21
	s_nop 0
	global_load_lds_dwordx4 v[174:175], off
	v_lshl_add_u64 v[174:175], s[38:39], 0, v[162:163]
	s_mov_b32 m0, s19
	s_nop 0
	global_load_lds_dwordx4 v[174:175], off
	v_lshl_add_u64 v[174:175], v[178:179], 0, s[8:9]
	s_mov_b32 m0, s59
	s_nop 0
	global_load_lds_dwordx4 v[174:175], off
	v_lshl_add_u64 v[174:175], v[180:181], 0, s[8:9]
	s_mov_b32 m0, s60
	s_nop 0
	global_load_lds_dwordx4 v[174:175], off
	s_waitcnt vmcnt(8)
	s_waitcnt lgkmcnt(0)
	s_barrier
	s_setprio 1
	s_waitcnt lgkmcnt(0)
	v_mfma_scale_f32_16x16x128_f8f6f4 v[78:81], v[2:9], v[190:197], v[78:81], v244, v189 op_sel_hi:[0,0,0]
	v_mfma_scale_f32_16x16x128_f8f6f4 v[74:77], v[10:17], v[190:197], v[74:77], v244, v189 op_sel_hi:[0,0,0]
	v_mfma_scale_f32_16x16x128_f8f6f4 v[70:73], v[2:9], v[198:205], v[70:73], v244, v189 op_sel_hi:[0,0,0]
	v_mfma_scale_f32_16x16x128_f8f6f4 v[66:69], v[10:17], v[198:205], v[66:69], v244, v189 op_sel_hi:[0,0,0]
	v_mfma_scale_f32_16x16x128_f8f6f4 v[46:49], v[2:9], v[206:213], v[46:49], v244, v189 op_sel_hi:[0,0,0]
	v_mfma_scale_f32_16x16x128_f8f6f4 v[42:45], v[10:17], v[206:213], v[42:45], v244, v189 op_sel_hi:[0,0,0]
	v_mfma_scale_f32_16x16x128_f8f6f4 v[38:41], v[2:9], v[214:221], v[38:41], v244, v189 op_sel_hi:[0,0,0]
	v_mfma_scale_f32_16x16x128_f8f6f4 v[34:37], v[10:17], v[214:221], v[34:37], v244, v189 op_sel_hi:[0,0,0]
	s_setprio 0
	s_setprio 1
	v_mfma_scale_f32_16x16x128_f8f6f4 v[90:93], v[18:25], v[190:197], v[90:93], v244, v189 op_sel_hi:[0,0,0]
	v_mfma_scale_f32_16x16x128_f8f6f4 v[94:97], v[26:33], v[190:197], v[94:97], v244, v189 op_sel_hi:[0,0,0]
	v_mfma_scale_f32_16x16x128_f8f6f4 v[82:85], v[18:25], v[198:205], v[82:85], v244, v189 op_sel_hi:[0,0,0]
	v_mfma_scale_f32_16x16x128_f8f6f4 v[86:89], v[26:33], v[198:205], v[86:89], v244, v189 op_sel_hi:[0,0,0]
	v_mfma_scale_f32_16x16x128_f8f6f4 v[58:61], v[18:25], v[206:213], v[58:61], v244, v189 op_sel_hi:[0,0,0]
	v_mfma_scale_f32_16x16x128_f8f6f4 v[62:65], v[26:33], v[206:213], v[62:65], v244, v189 op_sel_hi:[0,0,0]
	v_mfma_scale_f32_16x16x128_f8f6f4 v[50:53], v[18:25], v[214:221], v[50:53], v244, v189 op_sel_hi:[0,0,0]
	v_mfma_scale_f32_16x16x128_f8f6f4 v[54:57], v[26:33], v[214:221], v[54:57], v244, v189 op_sel_hi:[0,0,0]
	s_setprio 0
	s_barrier
	s_andn2_b64 vcc, exec, s[36:37]
	s_mov_b64 s[38:39], -1
	s_mov_b64 s[36:37], 0
	s_mov_b64 s[42:43], 0x100
	s_cbranch_vccz .LBB0_1144
	v_mov_b32_e32 v2, v182
	v_mov_b32_e32 v3, v183
	s_nop 15
	s_nop 15
	s_lshl_b32 s17, s28, 8
	v_lshlrev_b32_e32 v4, 4, v3
	s_add_i32 s17, s17, s57
	v_and_b32_e32 v4, 16, v4
	v_add3_u32 v2, s17, v2, v4
	s_lshl_b32 s17, s67, 8
	v_lshlrev_b32_e32 v3, 3, v3
	s_or_b32 s17, s17, s58
	v_and_b32_e32 v3, -16, v3
	v_add_u32_e32 v4, s17, v3
	v_ashrrev_i32_e32 v3, 31, v2
	v_lshlrev_b64 v[2:3], 11, v[2:3]
	v_ashrrev_i32_e32 v5, 31, v4
	v_lshl_add_u64 v[2:3], s[6:7], 0, v[2:3]
	v_lshl_add_u64 v[2:3], v[2:3], 0, v[4:5]
	v_cvt_pk_fp8_f32 v4, v158, v159
	v_cvt_pk_fp8_f32 v5, v154, v155
	v_cvt_pk_fp8_f32 v4, v160, v161 op_sel:[0,0,1]
	v_cvt_pk_fp8_f32 v5, v156, v157 op_sel:[0,0,1]
	v_cvt_pk_fp8_f32 v6, v150, v151
	v_cvt_pk_fp8_f32 v7, v146, v147
	v_cvt_pk_fp8_f32 v6, v152, v153 op_sel:[0,0,1]
	v_cvt_pk_fp8_f32 v7, v148, v149 op_sel:[0,0,1]
	s_nop 0
	v_permlane16_swap_b32_e32 v4, v6
	v_permlane16_swap_b32_e32 v5, v7
	global_store_dwordx4 v[2:3], v[4:7], off
	s_mov_b32 s67, s20
	s_mov_b32 s28, s16
	v_cvt_pk_fp8_f32 v4, v142, v143
	v_cvt_pk_fp8_f32 v5, v138, v139
	v_cvt_pk_fp8_f32 v4, v144, v145 op_sel:[0,0,1]
	v_cvt_pk_fp8_f32 v5, v140, v141 op_sel:[0,0,1]
	v_cvt_pk_fp8_f32 v6, v134, v135
	v_cvt_pk_fp8_f32 v7, v130, v131
	v_cvt_pk_fp8_f32 v6, v136, v137 op_sel:[0,0,1]
	s_mov_b64 s[30:31], s[26:27]
	v_cvt_pk_fp8_f32 v7, v132, v133 op_sel:[0,0,1]
	v_permlane16_swap_b32_e32 v4, v6
	v_lshl_add_u64 v[8:9], v[2:3], 0, s[4:5]
	v_permlane16_swap_b32_e32 v5, v7
	global_store_dwordx4 v[2:3], v[4:7], off offset:128
	s_mov_b64 s[34:35], s[24:25]
	s_nop 0
	v_cvt_pk_fp8_f32 v4, v126, v127
	v_cvt_pk_fp8_f32 v5, v122, v123
	v_cvt_pk_fp8_f32 v4, v128, v129 op_sel:[0,0,1]
	v_cvt_pk_fp8_f32 v5, v124, v125 op_sel:[0,0,1]
	v_cvt_pk_fp8_f32 v6, v118, v119
	v_cvt_pk_fp8_f32 v7, v114, v115
	v_cvt_pk_fp8_f32 v6, v120, v121 op_sel:[0,0,1]
	s_nop 0
	s_nop 0
	v_permlane16_swap_b32_e32 v4, v6
	v_cvt_pk_fp8_f32 v7, v116, v117 op_sel:[0,0,1]
	v_add_co_u32_e32 v10, vcc, s56, v2
	s_nop 0
	v_permlane16_swap_b32_e32 v5, v7
	v_addc_co_u32_e32 v11, vcc, 0, v3, vcc
	global_store_dwordx4 v[10:11], v[4:7], off
	s_nop 1
	v_cvt_pk_fp8_f32 v4, v110, v111
	v_cvt_pk_fp8_f32 v5, v106, v107
	v_cvt_pk_fp8_f32 v4, v112, v113 op_sel:[0,0,1]
	v_cvt_pk_fp8_f32 v5, v108, v109 op_sel:[0,0,1]
	v_cvt_pk_fp8_f32 v6, v102, v103
	v_cvt_pk_fp8_f32 v7, v98, v99
	v_cvt_pk_fp8_f32 v6, v104, v105 op_sel:[0,0,1]
	s_nop 0
	s_nop 0
	v_permlane16_swap_b32_e32 v4, v6
	v_cvt_pk_fp8_f32 v7, v100, v101 op_sel:[0,0,1]
	s_nop 0
	s_nop 0
	v_permlane16_swap_b32_e32 v5, v7
	global_store_dwordx4 v[8:9], v[4:7], off offset:128
	v_lshl_add_u64 v[8:9], v[2:3], 0, s[12:13]
	s_nop 0
	v_cvt_pk_fp8_f32 v4, v78, v79
	v_cvt_pk_fp8_f32 v5, v74, v75
	v_cvt_pk_fp8_f32 v4, v80, v81 op_sel:[0,0,1]
	v_cvt_pk_fp8_f32 v5, v76, v77 op_sel:[0,0,1]
	v_cvt_pk_fp8_f32 v6, v70, v71
	v_cvt_pk_fp8_f32 v7, v66, v67
	v_cvt_pk_fp8_f32 v6, v72, v73 op_sel:[0,0,1]
	s_nop 0
	s_nop 0
	v_permlane16_swap_b32_e32 v4, v6
	v_cvt_pk_fp8_f32 v7, v68, v69 op_sel:[0,0,1]
	v_add_co_u32_e32 v10, vcc, s65, v2
	s_nop 0
	v_permlane16_swap_b32_e32 v5, v7
	v_addc_co_u32_e32 v11, vcc, 0, v3, vcc
	global_store_dwordx4 v[10:11], v[4:7], off
	s_nop 1
	v_cvt_pk_fp8_f32 v4, v90, v91
	v_cvt_pk_fp8_f32 v5, v94, v95
	v_cvt_pk_fp8_f32 v4, v92, v93 op_sel:[0,0,1]
	v_cvt_pk_fp8_f32 v5, v96, v97 op_sel:[0,0,1]
	v_cvt_pk_fp8_f32 v6, v82, v83
	v_cvt_pk_fp8_f32 v7, v86, v87
	v_cvt_pk_fp8_f32 v6, v84, v85 op_sel:[0,0,1]
	s_nop 0
	s_nop 0
	v_permlane16_swap_b32_e32 v4, v6
	v_cvt_pk_fp8_f32 v7, v88, v89 op_sel:[0,0,1]
	s_nop 0
	s_nop 0
	v_permlane16_swap_b32_e32 v5, v7
	global_store_dwordx4 v[8:9], v[4:7], off offset:128
	v_lshl_add_u64 v[8:9], v[2:3], 0, s[14:15]
	v_add_co_u32_e32 v2, vcc, s66, v2
	v_cvt_pk_fp8_f32 v4, v46, v47
	v_cvt_pk_fp8_f32 v5, v42, v43
	v_cvt_pk_fp8_f32 v4, v48, v49 op_sel:[0,0,1]
	v_cvt_pk_fp8_f32 v5, v44, v45 op_sel:[0,0,1]
	v_cvt_pk_fp8_f32 v6, v38, v39
	v_cvt_pk_fp8_f32 v7, v34, v35
	v_addc_co_u32_e32 v3, vcc, 0, v3, vcc
	v_cvt_pk_fp8_f32 v6, v40, v41 op_sel:[0,0,1]
	s_and_b64 vcc, exec, s[22:23]
	v_cvt_pk_fp8_f32 v7, v36, v37 op_sel:[0,0,1]
	v_permlane16_swap_b32_e32 v4, v6
	s_nop 0
	v_permlane16_swap_b32_e32 v5, v7
	global_store_dwordx4 v[2:3], v[4:7], off
	v_cvt_pk_fp8_f32 v2, v58, v59
	v_cvt_pk_fp8_f32 v3, v62, v63
	v_cvt_pk_fp8_f32 v2, v60, v61 op_sel:[0,0,1]
	v_cvt_pk_fp8_f32 v3, v64, v65 op_sel:[0,0,1]
	v_cvt_pk_fp8_f32 v4, v50, v51
	v_cvt_pk_fp8_f32 v5, v54, v55
	v_cvt_pk_fp8_f32 v4, v52, v53 op_sel:[0,0,1]
	s_nop 0
	s_nop 0
	v_permlane16_swap_b32_e32 v2, v4
	v_cvt_pk_fp8_f32 v5, v56, v57 op_sel:[0,0,1]
	s_nop 0
	s_nop 0
	v_permlane16_swap_b32_e32 v3, v5
	global_store_dwordx4 v[8:9], v[2:5], off offset:128
	s_cbranch_vccz .LBB0_1139
	s_waitcnt vmcnt(0)
	s_cmpk_gt_u32 s11, 0xff
	s_cbranch_scc1 .LBB0_1148
	s_barrier
